# mixer chunk loop: one static s_setprio 1 for waves 4-7 (younger half), reset at loop exit
# speedup vs baseline: 1.0062x; 1.0062x over previous
.LBB0_448:
	s_setprio 0
	v_readlane_b32 s81, v255, 7
	s_add_i32 s93, s93, s81
	v_readlane_b32 s84, v255, 8
	s_cmpk_gt_i32 s93, 0xbf
	v_readlane_b32 s85, v255, 9
	v_readlane_b32 s86, v255, 10
	v_readlane_b32 s87, v255, 11
	s_mov_b32 s80, 0x800000
	s_waitcnt vmcnt(0)
	s_barrier
	s_cbranch_scc1 .LBB0_482

.LBB0_464:
	s_ashr_i32 s8, s24, 2
	s_add_i32 s24, s8, s78
	s_lshl_b32 s8, s79, 7
	s_and_b64 s[78:79], s[76:77], exec
	s_movk_i32 s9, 0x1500
	s_cselect_b32 s9, s9, 0x1800
	s_and_b64 s[6:7], exec, s[6:7]
	s_cselect_b32 s6, 0x900, s9
	s_lshl_b32 s2, s2, 6
	s_and_b32 s40, s2, 64
	s_add_i32 s7, s81, s8
	s_or_b32 s78, s7, s40
	s_ashr_i32 s7, s5, 31
	s_lshr_b32 s7, s7, 30
	s_add_i32 s7, s5, s7
	s_and_b32 s7, s7, 0x1ffffc
	s_sub_i32 s5, s5, s7
	s_lshl_b32 s84, s5, 11
	v_cndmask_b32_e64 v3, v111, v110, s[76:77]
	v_add_u32_e32 v3, s84, v3
	s_add_i32 s2, s80, s8
	v_mad_i64_i32 v[4:5], s[80:81], v3, s20, v[38:39]
	s_add_i32 s6, s6, s8
	s_mov_b32 s7, s3
	s_lshl_b64 s[80:81], s[2:3], 1
	s_mov_b32 m0, s19
	v_lshl_add_u64 v[6:7], v[4:5], 0, s[80:81]
	s_lshl_b64 s[6:7], s[6:7], 1
	v_cndmask_b32_e64 v3, v113, v112, s[76:77]
	s_waitcnt vmcnt(0) lgkmcnt(0)
	s_barrier
	global_load_lds_dwordx4 v[6:7], off
	v_lshl_add_u64 v[4:5], v[4:5], 0, s[6:7]
	s_mov_b32 m0, s82
	v_add_u32_e32 v3, s84, v3
	global_load_lds_dwordx4 v[4:5], off
	v_mad_i64_i32 v[4:5], s[86:87], v3, s20, v[38:39]
	s_add_i32 s85, s92, 0x1b600
	v_lshl_add_u64 v[6:7], v[4:5], 0, s[80:81]
	s_mov_b32 m0, s85
	s_add_i32 s86, s92, 0x1f600
	global_load_lds_dwordx4 v[6:7], off
	v_lshl_add_u64 v[4:5], v[4:5], 0, s[6:7]
	s_mov_b32 m0, s86
	v_cndmask_b32_e64 v3, v101, v100, s[76:77]
	global_load_lds_dwordx4 v[4:5], off
	v_add_u32_e32 v3, s84, v3
	v_mov_b64_e32 v[4:5], s[26:27]
	s_mov_b32 s79, s3
	v_mad_i64_i32 v[4:5], vcc, v3, s20, v[4:5]
	s_lshl_b64 s[78:79], s[78:79], 1
	s_add_i32 s87, s16, 0
	v_lshl_add_u64 v[4:5], v[4:5], 0, s[78:79]
	v_mov_b32_e32 v45, v195
	s_add_i32 s87, s87, 0x23600
	v_lshl_add_u64 v[4:5], v[4:5], 0, v[44:45]
	s_mov_b32 m0, s87
	v_mul_f32_e32 v144, 0x42800000, v2
	global_load_lds_dwordx4 v[4:5], off
	v_mul_f32_e32 v2, 0x42000000, v2
	v_exp_f32_e32 v18, v2
	s_ashr_i32 s9, s8, 31
	s_waitcnt vmcnt(0)
	s_lshl_b32 s2, s4, 13
	v_mad_i64_i32 v[2:3], s[4:5], s24, v242, v[42:43]
	v_lshl_add_u64 v[2:3], s[8:9], 1, v[2:3]
	s_lshl_b32 s4, s40, 1
	s_mov_b32 s5, s3
	v_mov_b32_e32 v22, 0
	v_lshl_add_u64 v[52:53], v[40:41], 0, s[78:79]
	v_sub_f32_e32 v45, 1.0, v140
	v_sub_f32_e32 v143, 1.0, v139
	v_lshl_add_u64 v[54:55], v[2:3], 0, s[4:5]
	v_mov_b32_e32 v47, v46
	s_mov_b32 s24, 0
	v_mov_b32_e32 v19, v18
	v_mov_b32_e32 v20, v18
	v_mov_b32_e32 v21, v18
	s_mov_b32 s4, 0
	v_mov_b32_e32 v23, v22
	v_mov_b32_e32 v24, v22
	v_mov_b32_e32 v25, v22
	v_mov_b32_e32 v26, v22
	v_mov_b32_e32 v27, v22
	v_mov_b32_e32 v28, v22
	v_mov_b32_e32 v29, v22
	v_mov_b32_e32 v30, v22
	v_mov_b32_e32 v31, v22
	v_mov_b32_e32 v32, v22
	v_mov_b32_e32 v33, v22
	v_mov_b32_e32 v34, v22
	v_mov_b32_e32 v35, v22
	v_mov_b32_e32 v36, v22
	v_mov_b32_e32 v37, v22
	v_readfirstlane_b32 s100, v0
	s_nop 3
	s_lshr_b32 s100, s100, 6
	s_cmp_ge_u32 s100, 4
	s_cbranch_scc0 .Lmx_prio_done
	s_setprio 1
.Lmx_prio_done:
	s_waitcnt vmcnt(0) lgkmcnt(0)
	s_barrier
	s_branch .LBB0_466
